# v23 + streaming (nt) policy on the HGRN2 scan's z loads (read once; keeps the phase-2 outputs in the caches for phase 3)
# baseline (speedup 1.0000x reference)
.LBB0_354:
	v_add_u32_e32 v8, 0x200, v8
	s_movk_i32 s70, 0x1fff
	v_cmp_lt_u32_e32 vcc, s70, v8
	ds_write_b32 v7, v69
	s_or_b64 s[58:59], vcc, s[58:59]
	v_add_u32_e32 v7, 0x800, v7
	s_andn2_b64 exec, exec, s[58:59]
	s_cbranch_execnz .LBB0_354
	s_or_b64 exec, exec, s[58:59]
	s_waitcnt vmcnt(0)
	v_sub_f32_e32 v4, v4, v2
	v_mul_f32_e32 v2, 0x3fb8aa3b, v4
	s_mov_b32 s46, 0x3fb8aa3b
	v_fma_f32 v7, v4, s46, -v2
	v_rndne_f32_e32 v8, v2
	v_fmac_f32_e32 v7, 0x32a5705f, v4
	v_sub_f32_e32 v2, v2, v8
	v_add_f32_e32 v2, v2, v7
	v_cvt_i32_f32_e32 v7, v8
	v_exp_f32_e32 v2, v2
	v_sub_f32_e32 v3, v5, v3
	s_and_b64 s[58:59], s[40:41], exec
	v_readlane_b32 s58, v254, 15
	v_ldexp_f32 v7, v2, v7
	v_mul_f32_e32 v2, 0x3fb8aa3b, v3
	v_fma_f32 v5, v3, s46, -v2
	v_rndne_f32_e32 v8, v2
	v_fmac_f32_e32 v5, 0x32a5705f, v3
	v_sub_f32_e32 v2, v2, v8
	v_add_f32_e32 v2, v2, v5
	v_exp_f32_e32 v5, v2
	v_cvt_i32_f32_e32 v8, v8
	s_mov_b32 s46, 0xc2ce8ed0
	v_cmp_ngt_f32_e32 vcc, s46, v4
	s_mov_b32 s89, 0x42b17218
	v_ldexp_f32 v5, v5, v8
	v_cndmask_b32_e32 v7, 0, v7, vcc
	v_cmp_ngt_f32_e32 vcc, s46, v3
	v_readlane_b32 s46, v254, 26
	s_cselect_b32 s58, s58, s46
	v_cndmask_b32_e32 v5, 0, v5, vcc
	v_cmp_nlt_f32_e32 vcc, s89, v3
	s_mulk_i32 s58, 0x1c00
	v_readlane_b32 s46, v254, 27
	v_cndmask_b32_e32 v3, v215, v5, vcc
	v_or_b32_e32 v5, s58, v6
	s_cselect_b32 s58, s60, s46
	s_mulk_i32 s58, 0x1c00
	v_readlane_b32 s46, v254, 28
	v_readlane_b32 s47, v254, 29
	v_or_b32_e32 v8, s58, v6
	s_cselect_b32 s58, s46, s47
	s_mulk_i32 s58, 0x1c00
	v_readlane_b32 s46, v254, 30
	v_readlane_b32 s47, v254, 31
	v_or_b32_e32 v9, s58, v6
	s_cselect_b32 s58, s46, s47
	s_mulk_i32 s58, 0x1c00
	v_readlane_b32 s46, v254, 32
	v_readlane_b32 s47, v254, 33
	v_or_b32_e32 v10, s58, v6
	s_cselect_b32 s58, s46, s47
	s_mulk_i32 s58, 0x1c00
	v_readlane_b32 s46, v254, 34
	v_readlane_b32 s47, v254, 35
	v_or_b32_e32 v11, s58, v6
	s_cselect_b32 s58, s46, s47
	s_mulk_i32 s58, 0x1c00
	v_readlane_b32 s46, v254, 36
	v_readlane_b32 s47, v254, 37
	v_or_b32_e32 v12, s58, v6
	s_cselect_b32 s58, s46, s47
	s_mulk_i32 s58, 0x1c00
	v_readlane_b32 s46, v254, 38
	v_readlane_b32 s47, v254, 39
	v_or_b32_e32 v13, s58, v6
	s_cselect_b32 s58, s46, s47
	s_mulk_i32 s58, 0x1c00
	v_add_f32_e32 v3, 1.0, v3
	v_or_b32_e32 v6, s58, v6
	v_lshlrev_b32_e32 v50, 1, v6
	v_div_scale_f32 v6, s[58:59], v3, v3, 1.0
	s_movk_i32 s58, 0x1800
	s_cselect_b32 s70, s58, 0x2000
	s_mov_b32 s58, 0x16600000
	s_cselect_b32 s58, s58, 0x1a600000
	s_add_u32 s82, s66, s58
	s_addc_u32 s83, s67, 0
	s_lshl_b32 s58, s5, 7
	s_and_b32 s88, s58, 0xfffff800
	s_and_b64 s[58:59], s[40:41], exec
	s_cselect_b32 s58, 0, 0x7c0
	s_or_b32 s58, s58, s88
	s_mul_hi_i32 s59, s58, 0x3800
	s_mulk_i32 s58, 0x3800
	s_add_u32 s86, s55, s58
	s_addc_u32 s87, s73, s59
	s_add_u32 s58, s86, s70
	s_addc_u32 s59, s87, 0
	s_add_u32 s84, s86, 0x1000
	s_addc_u32 s85, s87, 0
	v_lshlrev_b32_e32 v68, 1, v5
	s_add_u32 s86, s86, 0x2800
	v_lshlrev_b32_e32 v52, 1, v8
	v_lshlrev_b32_e32 v54, 1, v9
	v_lshlrev_b32_e32 v56, 1, v10
	v_lshlrev_b32_e32 v58, 1, v11
	v_lshlrev_b32_e32 v60, 1, v12
	v_lshlrev_b32_e32 v62, 1, v13
	s_addc_u32 s87, s87, 0
	global_load_dword v87, v68, s[58:59] nt
	global_load_dword v89, v68, s[84:85] nt
	global_load_dword v91, v68, s[86:87] nt
	global_load_dword v93, v52, s[58:59] nt
	global_load_dword v97, v52, s[84:85] nt
	global_load_dword v107, v52, s[86:87] nt
	global_load_dword v147, v54, s[84:85] nt
	global_load_dword v148, v54, s[86:87] nt
	global_load_dword v146, v54, s[58:59] nt
	global_load_dword v149, v56, s[58:59] nt
	global_load_dword v150, v56, s[84:85] nt
	global_load_dword v151, v56, s[86:87] nt
	global_load_dword v152, v58, s[58:59] nt
	global_load_dword v153, v58, s[84:85] nt
	global_load_dword v154, v58, s[86:87] nt
	global_load_dword v157, v60, s[86:87] nt
	global_load_dword v155, v60, s[58:59] nt
	global_load_dword v156, v60, s[84:85] nt
	global_load_dword v158, v62, s[58:59] nt
	global_load_dword v159, v62, s[84:85] nt
	global_load_dword v160, v62, s[86:87] nt
	global_load_dword v161, v50, s[58:59] nt
	global_load_dword v164, v50, s[84:85] nt
	global_load_dword v165, v50, s[86:87] nt
	v_rcp_f32_e32 v14, v6
	v_cmp_nlt_f32_e32 vcc, s89, v4
	v_readlane_b32 s46, v254, 40
	s_waitcnt lgkmcnt(0)
	v_fma_f32 v5, -v6, v14, 1.0
	v_cndmask_b32_e32 v4, v215, v7, vcc
	v_fmac_f32_e32 v14, v5, v14
	v_div_scale_f32 v5, vcc, 1.0, v3, 1.0
	v_mul_f32_e32 v7, v5, v14
	v_fma_f32 v8, -v6, v7, v5
	v_fmac_f32_e32 v7, v8, v14
	v_fma_f32 v5, -v6, v7, v5
	v_add_f32_e32 v4, 1.0, v4
	v_div_fmas_f32 v5, v5, v14, v7
	v_div_fixup_f32 v65, v5, v3, 1.0
	v_div_scale_f32 v3, s[58:59], v4, v4, 1.0
	v_rcp_f32_e32 v5, v3
	v_or_b32_e32 v6, s61, v189
	v_lshlrev_b32_e32 v6, 1, v6
	s_barrier
	v_fma_f32 v7, -v3, v5, 1.0
	v_fmac_f32_e32 v5, v7, v5
	v_div_scale_f32 v7, vcc, 1.0, v4, 1.0
	v_mul_f32_e32 v8, v7, v5
	v_fma_f32 v9, -v3, v8, v7
	v_fmac_f32_e32 v8, v9, v5
	v_fma_f32 v3, -v3, v8, v7
	v_div_fmas_f32 v3, v3, v5, v8
	v_div_fixup_f32 v64, v3, v4, 1.0
	v_cndmask_b32_e64 v3, v188, v187, s[40:41]
	v_lshlrev_b32_e32 v3, 11, v3
	v_mov_b32_e32 v2, 0
	v_or3_b32 v4, v6, s46, v3
	v_mov_b32_e32 v5, v69
	s_mov_b32 s89, 0
	v_pk_add_f32 v[108:109], v[64:65], 1.0 op_sel_hi:[1,0] neg_lo:[1,0] neg_hi:[1,0]
	v_mov_b32_e32 v53, v69
	v_mov_b32_e32 v55, v69
	v_mov_b32_e32 v57, v69
	v_mov_b32_e32 v59, v69
	v_mov_b32_e32 v61, v69
	v_mov_b32_e32 v63, v69
	v_mov_b32_e32 v51, v69
	v_lshl_add_u64 v[110:111], s[82:83], 0, v[4:5]
	s_movk_i32 s90, 0x780
	s_mov_b32 s91, 0
	v_mov_b32_e32 v3, v2
	v_mov_b32_e32 v4, v2
	v_mov_b32_e32 v5, v2
	v_mov_b32_e32 v6, v2
	v_mov_b32_e32 v7, v2
	v_mov_b32_e32 v8, v2
	v_mov_b32_e32 v9, v2
	v_mov_b32_e32 v10, v2
	v_mov_b32_e32 v11, v2
	v_mov_b32_e32 v12, v2
	v_mov_b32_e32 v13, v2
	v_mov_b32_e32 v14, v2
	v_mov_b32_e32 v15, v2
	v_mov_b32_e32 v16, v2
	v_mov_b32_e32 v17, v2
	v_mov_b32_e32 v18, v2
	v_mov_b32_e32 v19, v2
	v_mov_b32_e32 v20, v2
	v_mov_b32_e32 v21, v2
	v_mov_b32_e32 v22, v2
	v_mov_b32_e32 v23, v2
	v_mov_b32_e32 v24, v2
	v_mov_b32_e32 v25, v2
	v_mov_b32_e32 v26, v2
	v_mov_b32_e32 v27, v2
	v_mov_b32_e32 v28, v2
	v_mov_b32_e32 v29, v2
	v_mov_b32_e32 v30, v2
	v_mov_b32_e32 v31, v2
	v_mov_b32_e32 v32, v2
	v_mov_b32_e32 v33, v2
	s_branch .LBB0_357

.LBB0_361:
	v_cndmask_b32_e64 v47, v47, 0, s[44:45]
	v_cndmask_b32_e64 v166, v166, 0, s[44:45]
	v_add_f32_e32 v48, v48, v166
	v_add_f32_e32 v49, v49, v47
	v_cndmask_b32_e64 v47, v47, v49, s[8:9]
	v_cndmask_b32_e64 v48, v166, v48, s[8:9]
	v_add_f32_e32 v42, v42, v48
	v_add_f32_e32 v43, v43, v47
	v_cndmask_b32_e64 v43, v47, v43, s[10:11]
	v_cndmask_b32_e64 v42, v48, v42, s[10:11]
	v_add_f32_e32 v44, v44, v42
	v_add_f32_e32 v45, v45, v43
	v_cndmask_b32_e64 v43, v43, v45, s[12:13]
	v_cndmask_b32_e64 v42, v42, v44, s[12:13]
	v_add_f32_e32 v38, v38, v42
	v_add_f32_e32 v39, v39, v43
	v_cndmask_b32_e64 v39, v43, v39, s[14:15]
	v_cndmask_b32_e64 v38, v42, v38, s[14:15]
	v_add_f32_e32 v40, v40, v38
	v_add_f32_e32 v41, v41, v39
	v_cndmask_b32_e64 v39, v39, v41, s[16:17]
	v_cndmask_b32_e64 v38, v38, v40, s[16:17]
	v_add_f32_e32 v34, v34, v38
	v_add_f32_e32 v35, v35, v39
	v_cndmask_b32_e64 v35, v39, v35, s[18:19]
	v_cndmask_b32_e64 v34, v38, v34, s[18:19]
	v_add_f32_e32 v36, v36, v34
	v_add_f32_e32 v37, v37, v35
	v_cndmask_b32_e64 v47, v35, v37, s[20:21]
	v_cndmask_b32_e64 v166, v34, v36, s[20:21]
	v_add_f32_e32 v34, v144, v166
	v_add_f32_e32 v35, v145, v47
	v_exp_f32_e32 v34, v34
	v_exp_f32_e32 v35, v35
	v_pk_add_f32 v[120:121], v[108:109], v[120:121] neg_lo:[0,1] neg_hi:[0,1]
	v_pk_add_f32 v[36:37], v[108:109], v[126:127] neg_lo:[0,1] neg_hi:[0,1]
	v_rcp_f32_e32 v40, v34
	v_rcp_f32_e32 v41, v35
	v_add_f32_e32 v126, v140, v166
	v_add_f32_e32 v127, v141, v47
	v_exp_f32_e32 v126, v126
	v_pk_mul_f32 v[40:41], v[120:121], v[40:41]
	v_lshlrev_b32_e32 v120, 16, v89
	v_and_b32_e32 v121, 0xffff0000, v89
	v_exp_f32_e32 v127, v127
	v_pk_mul_f32 v[34:35], v[34:35], v[120:121]
	s_mul_i32 s58, s57, 0x880
	v_pk_add_f32 v[38:39], v[108:109], v[130:131] neg_lo:[0,1] neg_hi:[0,1]
	v_cvt_pk_bf16_f32 v120, v34, v35
	v_add_u32_e32 v121, s58, v192
	v_cvt_pk_bf16_f32 v130, v40, v41
	ds_write2st64_b32 v121, v120, v130 offset1:68
	v_lshlrev_b32_e32 v120, 16, v97
	v_and_b32_e32 v121, 0xffff0000, v97
	v_pk_mul_f32 v[120:121], v[126:127], v[120:121]
	v_rcp_f32_e32 v34, v126
	v_cvt_pk_bf16_f32 v130, v120, v121
	v_add_f32_e32 v120, v136, v166
	v_add_f32_e32 v121, v137, v47
	v_exp_f32_e32 v120, v120
	v_exp_f32_e32 v121, v121
	v_rcp_f32_e32 v35, v127
	v_pk_add_f32 v[122:123], v[108:109], v[122:123] neg_lo:[0,1] neg_hi:[0,1]
	v_rcp_f32_e32 v126, v120
	v_rcp_f32_e32 v127, v121
	v_pk_mul_f32 v[34:35], v[122:123], v[34:35]
	v_pk_add_f32 v[128:129], v[108:109], v[128:129] neg_lo:[0,1] neg_hi:[0,1]
	v_pk_add_f32 v[42:43], v[108:109], v[134:135] neg_lo:[0,1] neg_hi:[0,1]
	v_cvt_pk_bf16_f32 v134, v34, v35
	v_mov_b32_e32 v123, v34
	v_mov_b32_e32 v34, v41
	v_mov_b32_e32 v122, v40
	v_pk_mul_f32 v[40:41], v[46:47], v[34:35] op_sel_hi:[0,1]
	v_pk_mul_f32 v[34:35], v[128:129], v[126:127]
	v_lshlrev_b32_e32 v126, 16, v147
	v_and_b32_e32 v127, 0xffff0000, v147
	v_pk_mul_f32 v[120:121], v[120:121], v[126:127]
	v_add_f32_e32 v126, v132, v166
	v_add_f32_e32 v127, v133, v47
	v_exp_f32_e32 v126, v126
	v_exp_f32_e32 v127, v127
	s_mul_i32 s58, s60, 0x110
	v_add_u32_e32 v131, s58, v192
	v_cvt_pk_bf16_f32 v120, v120, v121
	ds_write2_b32 v131, v130, v120 offset1:68
	v_rcp_f32_e32 v120, v126
	v_rcp_f32_e32 v121, v127
	v_cvt_pk_bf16_f32 v128, v34, v35
	v_add_u32_e32 v130, 0x4400, v131
	ds_write2_b32 v130, v134, v128 offset1:68
	v_pk_mul_f32 v[36:37], v[36:37], v[120:121]
	v_lshlrev_b32_e32 v120, 16, v150
	v_and_b32_e32 v121, 0xffff0000, v150
	v_pk_mul_f32 v[120:121], v[126:127], v[120:121]
	v_cvt_pk_bf16_f32 v133, v36, v37
	v_cvt_pk_bf16_f32 v132, v120, v121
	v_add_f32_e32 v120, v124, v166
	v_add_f32_e32 v121, v125, v47
	v_exp_f32_e32 v120, v120
	v_exp_f32_e32 v121, v121
	v_mov_b32_e32 v124, v34
	v_mov_b32_e32 v125, v36
	v_rcp_f32_e32 v126, v120
	v_rcp_f32_e32 v127, v121
	v_mov_b32_e32 v36, v35
	v_pk_mul_f32 v[128:129], v[46:47], v[36:37] op_sel_hi:[0,1]
	v_lshlrev_b32_e32 v36, 16, v153
	v_pk_mul_f32 v[34:35], v[38:39], v[126:127]
	v_add_f32_e32 v38, v118, v166
	v_add_f32_e32 v39, v119, v47
	v_exp_f32_e32 v38, v38
	v_exp_f32_e32 v39, v39
	v_and_b32_e32 v37, 0xffff0000, v153
	v_pk_mul_f32 v[36:37], v[120:121], v[36:37]
	v_pk_add_f32 v[44:45], v[108:109], v[138:139] neg_lo:[0,1] neg_hi:[0,1]
	v_cvt_pk_bf16_f32 v118, v36, v37
	v_rcp_f32_e32 v36, v38
	v_rcp_f32_e32 v37, v39
	ds_write2_b32 v131, v132, v118 offset0:136 offset1:204
	v_cvt_pk_bf16_f32 v118, v34, v35
	ds_write2_b32 v130, v133, v118 offset0:136 offset1:204
	v_pk_mul_f32 v[36:37], v[42:43], v[36:37]
	v_lshlrev_b32_e32 v42, 16, v156
	v_and_b32_e32 v43, 0xffff0000, v156
	v_pk_mul_f32 v[38:39], v[38:39], v[42:43]
	v_cvt_pk_bf16_f32 v121, v36, v37
	v_cvt_pk_bf16_f32 v120, v38, v39
	v_add_f32_e32 v38, v114, v166
	v_add_f32_e32 v39, v115, v47
	v_exp_f32_e32 v38, v38
	v_exp_f32_e32 v39, v39
	v_mov_b32_e32 v43, v36
	v_mov_b32_e32 v36, v35
	v_pk_mul_f32 v[118:119], v[46:47], v[36:37] op_sel_hi:[0,1]
	v_lshlrev_b32_e32 v36, 16, v159
	v_and_b32_e32 v37, 0xffff0000, v159
	v_pk_mul_f32 v[36:37], v[38:39], v[36:37]
	v_rcp_f32_e32 v114, v38
	v_cvt_pk_bf16_f32 v38, v36, v37
	v_add_f32_e32 v36, v112, v166
	v_add_f32_e32 v37, v113, v47
	v_rcp_f32_e32 v115, v39
	v_exp_f32_e32 v36, v36
	v_exp_f32_e32 v37, v37
	v_add_u32_e32 v39, 0x400, v131
	v_mov_b32_e32 v42, v34
	v_pk_mul_f32 v[34:35], v[44:45], v[114:115]
	ds_write2_b32 v39, v120, v38 offset0:16 offset1:84
	v_rcp_f32_e32 v38, v36
	v_rcp_f32_e32 v39, v37
	v_cvt_pk_bf16_f32 v44, v34, v35
	v_add_u32_e32 v45, 0x4800, v131
	ds_write2_b32 v45, v121, v44 offset0:16 offset1:84
	v_lshlrev_b32_e32 v44, 16, v164
	v_and_b32_e32 v45, 0xffff0000, v164
	v_pk_add_f32 v[48:49], v[108:109], v[142:143] neg_lo:[0,1] neg_hi:[0,1]
	v_pk_mul_f32 v[36:37], v[36:37], v[44:45]
	v_pk_mul_f32 v[38:39], v[48:49], v[38:39]
	v_cvt_pk_bf16_f32 v36, v36, v37
	ds_write_b32 v131, v36 offset:1632
	v_cvt_pk_bf16_f32 v36, v38, v39
	ds_write_b32 v131, v36 offset:19040
	v_mov_b32_e32 v36, v34
	v_mov_b32_e32 v37, v38
	v_pk_mul_f32 v[122:123], v[116:117], v[122:123] op_sel_hi:[0,1]
	v_pk_mul_f32 v[124:125], v[116:117], v[124:125] op_sel_hi:[0,1]
	v_pk_mul_f32 v[42:43], v[116:117], v[42:43] op_sel_hi:[0,1]
	v_pk_mul_f32 v[44:45], v[116:117], v[36:37] op_sel_hi:[0,1]
	v_mov_b32_e32 v38, v35
	v_pk_mul_f32 v[38:39], v[46:47], v[38:39] op_sel_hi:[0,1]
	v_cvt_pk_bf16_f32 v34, v122, v123
	v_cvt_pk_bf16_f32 v35, v124, v125
	v_cvt_pk_bf16_f32 v36, v42, v43
	v_cvt_pk_bf16_f32 v37, v44, v45
	ds_write_b128 v204, v[34:37] offset:34816
	v_cvt_pk_bf16_f32 v34, v40, v41
	v_cvt_pk_bf16_f32 v35, v128, v129
	v_cvt_pk_bf16_f32 v36, v118, v119
	v_cvt_pk_bf16_f32 v37, v38, v39
	s_cmpk_eq_i32 s90, 0xffc0
	ds_write_b128 v204, v[34:37] offset:34960
	s_cbranch_scc1 .LBB0_363
	s_add_i32 s61, s89, 64
	s_and_b64 s[58:59], s[40:41], exec
	s_cselect_b32 s58, s61, s90
	s_add_i32 s58, s58, s88
	s_mul_hi_i32 s59, s58, 0x3800
	s_mulk_i32 s58, 0x3800
	s_add_u32 s58, s55, s58
	s_addc_u32 s59, s73, s59
	s_add_u32 s86, s58, s70
	s_addc_u32 s87, s59, 0
	s_add_u32 s84, s58, 0x1000
	s_addc_u32 s85, s59, 0
	s_add_u32 s82, s58, 0x2800
	v_lshl_add_u64 v[34:35], s[86:87], 0, v[68:69]
	s_addc_u32 s83, s59, 0
	global_load_dword v87, v[34:35], off nt
	v_lshl_add_u64 v[34:35], s[84:85], 0, v[68:69]
	global_load_dword v89, v[34:35], off nt
	v_lshl_add_u64 v[34:35], s[82:83], 0, v[68:69]
	global_load_dword v91, v[34:35], off nt
	v_lshl_add_u64 v[34:35], s[86:87], 0, v[52:53]
	global_load_dword v93, v[34:35], off nt
	v_lshl_add_u64 v[34:35], s[84:85], 0, v[52:53]
	global_load_dword v97, v[34:35], off nt
	v_lshl_add_u64 v[34:35], s[82:83], 0, v[52:53]
	global_load_dword v107, v[34:35], off nt
	v_lshl_add_u64 v[34:35], s[86:87], 0, v[54:55]
	global_load_dword v146, v[34:35], off nt
	v_lshl_add_u64 v[34:35], s[84:85], 0, v[54:55]
	global_load_dword v147, v[34:35], off nt
	v_lshl_add_u64 v[34:35], s[82:83], 0, v[54:55]
	global_load_dword v148, v[34:35], off nt
	v_lshl_add_u64 v[34:35], s[86:87], 0, v[56:57]
	global_load_dword v149, v[34:35], off nt
	v_lshl_add_u64 v[34:35], s[84:85], 0, v[56:57]
	global_load_dword v150, v[34:35], off nt
	v_lshl_add_u64 v[34:35], s[82:83], 0, v[56:57]
	global_load_dword v151, v[34:35], off nt
	v_lshl_add_u64 v[34:35], s[86:87], 0, v[58:59]
	global_load_dword v152, v[34:35], off nt
	v_lshl_add_u64 v[34:35], s[84:85], 0, v[58:59]
	global_load_dword v153, v[34:35], off nt
	v_lshl_add_u64 v[34:35], s[82:83], 0, v[58:59]
	global_load_dword v154, v[34:35], off nt
	v_lshl_add_u64 v[34:35], s[86:87], 0, v[60:61]
	global_load_dword v155, v[34:35], off nt
	v_lshl_add_u64 v[34:35], s[84:85], 0, v[60:61]
	global_load_dword v156, v[34:35], off nt
	v_lshl_add_u64 v[34:35], s[82:83], 0, v[60:61]
	global_load_dword v157, v[34:35], off nt
	v_lshl_add_u64 v[34:35], s[86:87], 0, v[62:63]
	global_load_dword v158, v[34:35], off nt
	v_lshl_add_u64 v[34:35], s[84:85], 0, v[62:63]
	global_load_dword v159, v[34:35], off nt
	v_lshl_add_u64 v[34:35], s[82:83], 0, v[62:63]
	global_load_dword v160, v[34:35], off nt
	v_lshl_add_u64 v[34:35], s[86:87], 0, v[50:51]
	global_load_dword v161, v[34:35], off nt
	v_lshl_add_u64 v[34:35], s[84:85], 0, v[50:51]
	global_load_dword v164, v[34:35], off nt
	v_lshl_add_u64 v[34:35], s[82:83], 0, v[50:51]
	global_load_dword v165, v[34:35], off nt
